# MoE2 dynamic queue: next unit index requested one unit ahead (atomic latency hidden behind the unit)
# baseline (speedup 1.0000x reference)
; #define LAS __attribute__((address_space(3)))
; template <int MODE>
; __device__ __forceinline__ int moe_gemm(const Args& a, unsigned char* lds_g, int tid, int idx0) {
;     constexpr int K = MODE == 1 ? D : DE, NT = K / 64;
;     ...
;     const int w = __builtin_amdgcn_readfirstlane(tid >> 6);
;     const int wm = w >> 1, wn = w & 1, hh = wm >> 1, wr = wm & 1;
;     const int* cum = (const int*)(lds_g + MG_CUM); const unsigned* ctl = (const unsigned*)(a.ws + WS_CTL);
;     const int T = cum[NEXP], x = blockIdx.x & 7;
;     const int jl = (int)(blockIdx.x >> 3), nl = (int)(gridDim.x >> 3);
;     for (int it = 0;; ++it) {
;         int idx;
;         if (MODE == 1) idx = jl + nl * it; else idx = moe_pull(a, lds_g, w, x);
;         if (idx >= T) return idx;
;         const int ti = idx;
;         const int nt = x;
;     ...
;         else {
; #pragma unroll
;             for (int q = 0; q < 2; ++q) aofs[q] = (unsigned)((128 * q + (tidu >> 2)) * DE + 16 * (tidu & 3));
;             aofs[2] = aofs[3] = 0u;
;             rsA = __builtin_amdgcn_make_buffer_rsrc((void*)((const unsigned char*)(a.ws + WS_HM) + (size_t)256 * ti * DE), 0, 0x7fffffff, 0x00020000);
;             rsB = __builtin_amdgcn_make_buffer_rsrc((void*)(a.in[I_W2] + (size_t)e * DE * D), 0, 0x7fffffff, 0x00020000); rsB3 = rsB;
;             bofs = (unsigned)(bk * D + 256 * nt + 4 * bp) * 4u; bwr0 = MH_BROW * (2 * (bk & 3) + (bk >> 2)) + 2 * (128 * (bp >> 5) + 32 * ((bp & 31) >> 3) + 16 * (bp & 1) + 4 * ((bp >> 1) & 3)); }
;         const LAS unsigned char* blane = (const LAS unsigned char*)lds_g + MH_B + mhb_off(16 * (lane >> 5) + 8 * ((lane >> 4) & 1) + 2 * ((lane & 15) >> 2), 16 * wn + ((lane & 3) >> 1)) + 8 * (lane & 1);
.LBB0_1185:
	s_mov_b32 s101, 0
	s_lshl_b32 s0, s83, 8
	s_and_b32 s4, s0, 0x700
	s_add_u32 s5, s84, s4
	v_mbcnt_lo_u32_b32 v0, -1, 0
	v_mbcnt_hi_u32_b32 v0, -1, v0
	v_readlane_b32 s0, v249, 1
	s_addc_u32 s6, s85, 0
	s_add_u32 s8, s5, 0x8000
	v_or_b32_e32 v0, s0, v0
	s_addc_u32 s9, s6, 0
	v_readfirstlane_b32 s7, v0
	s_lshr_b32 s16, s7, 6
	s_bfe_u32 s17, s7, 0x10006
	s_lshr_b32 s18, s7, 8
	s_add_i32 s0, 0, 0x22880
	s_cmp_lt_u32 s7, 64
	v_mov_b32_e32 v0, s0
	s_cselect_b64 s[0:1], -1, 0
	s_lshl_b32 s16, s16, 11
	s_or_b32 s26, s16, s4
	s_lshr_b32 s4, s7, 5
	s_and_b32 s4, s4, 6
	s_add_i32 s27, s4, s18
	s_lshl_b32 s4, s17, 8
	s_lshr_b32 s19, s7, 1
	s_add_i32 s29, s4, 0
	s_ashr_i32 s4, s7, 5
	s_and_b32 s19, s19, 64
	s_and_b32 s30, s4, -2
	s_lshl_b32 s4, s18, 14
	s_and_b32 s22, s7, 0xffffc0
	s_lshl_b32 s23, s19, 7
	s_add_i32 s29, s29, 0x10000
	s_add_i32 s31, s4, 0
	s_lshl_b32 s4, s17, 7
	s_lshl_b32 s7, s18, 7
	ds_read_b32 v190, v0
	s_add_u32 s4, s5, s4
	s_addc_u32 s5, s6, 0
	s_add_u32 s33, s4, 0x33200000
	s_addc_u32 s34, s5, 0
	v_cndmask_b32_e64 v0, 0, 1, s[0:1]
	s_add_i32 s36, 0, 0x22900
	s_mulk_i32 s27, 0x210
	s_mov_b32 s28, 0x10000
	s_or_b32 s35, s7, s19
	v_cmp_ne_u32_e64 s[0:1], 1, v0
	v_mov_b32_e32 v189, 0
	v_mov_b32_e32 v191, s36
	s_brev_b32 s37, 1
	s_add_i32 s38, 0, 0x2287c
	s_movk_i32 s39, 0x3c0
	s_movk_i32 s42, 0xfc00
	s_mov_b32 s7, 0x20000
	s_brev_b32 s6, -2
	s_mov_b32 s43, 0x30000
	s_mov_b32 s44, 0x40000
	s_mov_b32 s45, 0x50000
	s_mov_b32 s46, 0x60000
	s_mov_b32 s47, 0x70000
	s_mov_b32 s48, 0x80000
	s_mov_b32 s49, 0x90000
	s_mov_b32 s50, 0xa0000
	s_mov_b32 s51, 0xb0000
	s_mov_b32 s52, 0xc0000
	s_mov_b32 s53, 0xd0000
	s_mov_b32 s54, 0xe0000
	s_mov_b32 s55, 0xf0000
	s_mov_b32 s56, 0x8000
	s_mov_b32 s57, 0x18000
	s_branch .LBB0_1187

; __device__ __forceinline__ int fresh_lane() { int l; asm volatile("v_mbcnt_lo_u32_b32 %0, -1, 0\n\tv_mbcnt_hi_u32_b32 %0, -1, %0" : "=v"(l)); __builtin_assume(l >= 0 && l < 64); return l; }
; __device__ __forceinline__ int moe_pull(const Args& a, unsigned char* lds_g, int w, int x) {
;     int* slot = (int*)(lds_g + MG_CUM + 256);
;     __syncthreads();
;     if (w == 0 && fresh_lane() == 0) *slot = (int)__hip_atomic_fetch_add((unsigned*)(a.ws + WS_CTL) + CW_Q + 64 * x, 1u, __ATOMIC_RELAXED, __HIP_MEMORY_SCOPE_AGENT);
;     __syncthreads();
;     return __builtin_amdgcn_readfirstlane(*slot);
; }
.LBB0_1187:
	s_and_b64 vcc, exec, s[0:1]
	s_waitcnt lgkmcnt(0)
	s_barrier
	s_cbranch_vccnz .LBB0_1193
	v_mbcnt_lo_u32_b32 v0, -1, 0
	v_mbcnt_hi_u32_b32 v0, -1, v0
	s_nop 0
	v_cmp_eq_u32_e32 vcc, 0, v0
	s_and_saveexec_b64 s[4:5], vcc
	s_cbranch_execz .LBB0_1192
	s_mov_b64 s[18:19], exec
	v_mbcnt_lo_u32_b32 v0, s18, 0
	v_mbcnt_hi_u32_b32 v0, s19, v0
	v_cmp_eq_u32_e32 vcc, 0, v0
	s_and_saveexec_b64 s[16:17], vcc
	s_cbranch_execz .LBB0_1191
	s_cmp_eq_u32 s101, 0x5a5a
	s_cbranch_scc1 .Lq_have
	s_bcnt1_i32_b64 s18, s[18:19]
	v_mov_b32_e32 v1, s18
	global_atomic_add v1, v189, v1, s[8:9] sc0
	s_branch .Lq_got
.Lq_have:
	s_waitcnt vmcnt(0)
	v_mov_b32_e32 v1, v250
.Lq_got:
.LBB0_1191:
	s_or_b64 exec, exec, s[16:17]
	s_waitcnt vmcnt(0)
	v_readfirstlane_b32 s16, v1
	v_mov_b32_e32 v1, s36
	s_nop 0
	v_add_u32_e32 v0, s16, v0
	ds_write_b32 v1, v0

; __device__ __forceinline__ int fresh_lane() { int l; asm volatile("v_mbcnt_lo_u32_b32 %0, -1, 0\n\tv_mbcnt_hi_u32_b32 %0, -1, %0" : "=v"(l)); __builtin_assume(l >= 0 && l < 64); return l; }
; template <int MODE>
; __device__ __forceinline__ int moe_gemm(const Args& a, unsigned char* lds_g, int tid, int idx0) {
;     ...
;             if (w == 0) { unsigned* tc = (unsigned*)(a.ws + WS_CTL) + CW_TC + 64 * ti; unsigned spins = 0;
;                 while ((unsigned)__builtin_amdgcn_readfirstlane(__hip_atomic_load(tc, __ATOMIC_RELAXED, __HIP_MEMORY_SCOPE_AGENT)) < 64u) {
;                     __builtin_amdgcn_s_sleep(2);
;                     if (++spins > (1u << 22)) { if (fresh_lane() == 0) __hip_atomic_store((unsigned*)(a.ws + WS_CTL) + 1, 0x900u + (unsigned)ti, __ATOMIC_RELAXED, __HIP_MEMORY_SCOPE_AGENT); break; } }
;                 __builtin_amdgcn_fence(__ATOMIC_ACQUIRE, "agent");
;                 asm volatile("s_waitcnt vmcnt(0)" ::: "memory"); }
.LBB0_1207:
	s_waitcnt vmcnt(0)
	s_waitcnt vmcnt(0)
	s_mov_b64 exec, 1
	v_mov_b32_e32 v251, 1
	global_atomic_add v250, v189, v251, s[8:9] sc0
	s_mov_b64 exec, -1
	s_mov_b32 s101, 0x5a5a

; __global__ void __launch_bounds__(NTHR, 2) fwd_kernel(Args args) {
	.amdhsa_kernel _Z10fwd_kernel4Args
		.amdhsa_group_segment_fixed_size 0
		.amdhsa_private_segment_fixed_size 0
		.amdhsa_kernarg_size 496
		.amdhsa_user_sgpr_count 2
		.amdhsa_user_sgpr_dispatch_ptr 0
		.amdhsa_user_sgpr_queue_ptr 0
		.amdhsa_user_sgpr_kernarg_segment_ptr 1
		.amdhsa_user_sgpr_dispatch_id 0
		.amdhsa_user_sgpr_kernarg_preload_length 0
		.amdhsa_user_sgpr_kernarg_preload_offset 0
		.amdhsa_user_sgpr_private_segment_size 0
		.amdhsa_uses_dynamic_stack 0
		.amdhsa_enable_private_segment 0
		.amdhsa_system_sgpr_workgroup_id_x 1
		.amdhsa_system_sgpr_workgroup_id_y 0
		.amdhsa_system_sgpr_workgroup_id_z 0
		.amdhsa_system_sgpr_workgroup_info 0
		.amdhsa_system_vgpr_workitem_id 0
		.amdhsa_next_free_vgpr 252
		.amdhsa_next_free_sgpr 102
		.amdhsa_accum_offset 252
		.amdhsa_reserve_vcc 1
		.amdhsa_float_round_mode_32 0
		.amdhsa_float_round_mode_16_64 0
		.amdhsa_float_denorm_mode_32 3
		.amdhsa_float_denorm_mode_16_64 3
		.amdhsa_dx10_clamp 1
		.amdhsa_ieee_mode 1
		.amdhsa_fp16_overflow 0
		.amdhsa_tg_split 0
		.amdhsa_exception_fp_ieee_invalid_op 0
		.amdhsa_exception_fp_denorm_src 0
		.amdhsa_exception_fp_ieee_div_zero 0
		.amdhsa_exception_fp_ieee_overflow 0
		.amdhsa_exception_fp_ieee_underflow 0
		.amdhsa_exception_fp_ieee_inexact 0
		.amdhsa_exception_int_div_zero 0
	.end_amdhsa_kernel

; __global__ void __launch_bounds__(NTHR, 2) fwd_kernel(Args args) {
amdhsa.kernels:
  - .agpr_count:     0
    .args:
      - .offset:         0
        .size:           240
        .value_kind:     by_value
      - .offset:         240
        .size:           4
        .value_kind:     hidden_block_count_x
      - .offset:         244
        .size:           4
        .value_kind:     hidden_block_count_y
      - .offset:         248
        .size:           4
        .value_kind:     hidden_block_count_z
      - .offset:         252
        .size:           2
        .value_kind:     hidden_group_size_x
      - .offset:         254
        .size:           2
        .value_kind:     hidden_group_size_y
      - .offset:         256
        .size:           2
        .value_kind:     hidden_group_size_z
      - .offset:         258
        .size:           2
        .value_kind:     hidden_remainder_x
      - .offset:         260
        .size:           2
        .value_kind:     hidden_remainder_y
      - .offset:         262
        .size:           2
        .value_kind:     hidden_remainder_z
      - .offset:         280
        .size:           8
        .value_kind:     hidden_global_offset_x
      - .offset:         288
        .size:           8
        .value_kind:     hidden_global_offset_y
      - .offset:         296
        .size:           8
        .value_kind:     hidden_global_offset_z
      - .offset:         304
        .size:           2
        .value_kind:     hidden_grid_dims
      - .offset:         360
        .size:           4
        .value_kind:     hidden_dynamic_lds_size
    .group_segment_fixed_size: 0
    .kernarg_segment_align: 8
    .kernarg_segment_size: 496
    .language:       OpenCL C
    .language_version:
      - 2
      - 0
    .max_flat_workgroup_size: 512
    .name:           _Z10fwd_kernel4Args
    .private_segment_fixed_size: 0
    .sgpr_count:     108
    .sgpr_spill_count: 42
    .symbol:         _Z10fwd_kernel4Args.kd
    .uniform_work_group_size: 1
    .uses_dynamic_stack: false
    .vgpr_count:     252
    .vgpr_spill_count: 0
    .wavefront_size: 64
